# stream: per-block rotation of the 1KiB chunk order within a row (by blk>>3) on top of rotated wave-row assignment
# baseline (speedup 1.0000x reference)
.LBB1_2:
	s_or_b64 exec, exec, s[0:1]
	s_lshr_b32 s8, s3, 6
	s_add_i32 s8, s8, s2
	s_and_b32 s8, s8, 15
	s_lshl_b32 s0, s2, 7
	v_and_b32_e32 v24, 63, v0
	s_add_i32 s9, s8, s0
	s_waitcnt lgkmcnt(0)
	s_and_b32 s1, s5, 0xffff
	s_mov_b32 s3, 0x20000
	s_brev_b32 s2, 16
	s_mov_b32 s0, s4
	v_lshlrev_b32_e32 v25, 4, v24
	s_lshr_b32 s11, s9, 10
	s_and_b32 s11, s11, 3
	s_add_i32 s12, s11, 0
	s_and_b32 s12, s12, 3
	s_lshl_b32 s12, s12, 10
	v_add_u32_e32 v67, s12, v25
	s_add_i32 s12, s11, 1
	s_and_b32 s12, s12, 3
	s_lshl_b32 s12, s12, 10
	v_add_u32_e32 v68, s12, v25
	s_add_i32 s12, s11, 2
	s_and_b32 s12, s12, 3
	s_lshl_b32 s12, s12, 10
	v_add_u32_e32 v69, s12, v25
	s_add_i32 s12, s11, 3
	s_and_b32 s12, s12, 3
	s_lshl_b32 s12, s12, 10
	v_add_u32_e32 v70, s12, v25
	s_lshl_b32 s4, s9, 12
	buffer_load_dwordx4 v[26:29], v68, s[0:3], s4 offen nt
	buffer_load_dwordx4 v[30:33], v67, s[0:3], s4 offen nt
	buffer_load_dwordx4 v[34:37], v69, s[0:3], s4 offen nt
	s_add_i32 s5, s4, 0x10000
	buffer_load_dwordx4 v[38:41], v68, s[0:3], s5 offen nt
	buffer_load_dwordx4 v[42:45], v67, s[0:3], s5 offen nt
	buffer_load_dwordx4 v[16:19], v70, s[0:3], s4 offen nt
	s_add_i32 s10, s4, 0x20000
	buffer_load_dwordx4 v[46:49], v69, s[0:3], s5 offen nt
	buffer_load_dwordx4 v[20:23], v70, s[0:3], s5 offen nt
	s_barrier
	buffer_load_dwordx4 v[50:53], v68, s[0:3], s10 offen nt
	buffer_load_dwordx4 v[54:57], v67, s[0:3], s10 offen nt
	ds_read_b128 v[4:7], v68
	ds_read_b128 v[0:3], v67
	ds_read_b128 v[12:15], v69
	ds_read_b128 v[8:11], v70
	s_add_i32 s5, s4, 0x30000
	v_cmp_gt_u32_e32 vcc, 8, v24
	s_waitcnt vmcnt(9) lgkmcnt(3)
	v_pk_mul_f32 v[28:29], v[6:7], v[28:29]
	v_pk_mul_f32 v[26:27], v[4:5], v[26:27]
	s_waitcnt vmcnt(8) lgkmcnt(2)
	v_pk_fma_f32 v[32:33], v[2:3], v[32:33], v[28:29]
	v_pk_fma_f32 v[30:31], v[0:1], v[30:31], v[26:27]
	buffer_load_dwordx4 v[26:29], v68, s[0:3], s5 offen nt
	s_waitcnt vmcnt(8) lgkmcnt(1)
	v_pk_fma_f32 v[58:59], v[14:15], v[36:37], v[32:33]
	v_pk_fma_f32 v[60:61], v[12:13], v[34:35], v[30:31]
	buffer_load_dwordx4 v[30:33], v67, s[0:3], s5 offen nt
	s_waitcnt vmcnt(8)
	v_pk_mul_f32 v[34:35], v[6:7], v[40:41]
	v_pk_mul_f32 v[36:37], v[4:5], v[38:39]
	s_waitcnt vmcnt(7)
	v_pk_fma_f32 v[44:45], v[2:3], v[44:45], v[34:35]
	v_pk_fma_f32 v[42:43], v[0:1], v[42:43], v[36:37]
	buffer_load_dwordx4 v[34:37], v69, s[0:3], s10 offen nt
	s_waitcnt vmcnt(4)
	v_pk_mul_f32 v[38:39], v[6:7], v[52:53]
	v_pk_mul_f32 v[40:41], v[4:5], v[50:51]
	s_waitcnt vmcnt(3)
	v_pk_fma_f32 v[50:51], v[2:3], v[56:57], v[38:39]
	v_pk_fma_f32 v[52:53], v[0:1], v[54:55], v[40:41]
	buffer_load_dwordx4 v[38:41], v70, s[0:3], s10 offen nt
	v_pk_fma_f32 v[48:49], v[14:15], v[48:49], v[44:45]
	v_pk_fma_f32 v[46:47], v[12:13], v[46:47], v[42:43]
	s_waitcnt lgkmcnt(0)
	v_pk_fma_f32 v[18:19], v[10:11], v[18:19], v[58:59]
	v_pk_fma_f32 v[16:17], v[8:9], v[16:17], v[60:61]
	v_add_f32_e32 v61, v18, v19
	v_add_f32_e32 v60, v16, v17
	v_pk_fma_f32 v[16:17], v[10:11], v[22:23], v[48:49]
	v_pk_fma_f32 v[18:19], v[8:9], v[20:21], v[46:47]
	v_add_f32_e32 v16, v16, v17
	v_add_f32_e32 v18, v18, v19
	v_add_f32_e32 v60, v60, v61
	v_add_f32_e32 v16, v18, v16
	s_add_i32 s10, s4, 0x50000
	s_waitcnt vmcnt(3)
	v_pk_mul_f32 v[28:29], v[6:7], v[28:29]
	v_pk_mul_f32 v[26:27], v[4:5], v[26:27]
	v_add_f32_dpp v16, v16, v16 quad_perm:[1,0,3,2] row_mask:0xf bank_mask:0xf bound_ctrl:1
	s_waitcnt vmcnt(2)
	v_pk_fma_f32 v[54:55], v[2:3], v[32:33], v[28:29]
	v_pk_fma_f32 v[56:57], v[0:1], v[30:31], v[26:27]
	buffer_load_dwordx4 v[26:29], v69, s[0:3], s5 offen nt
	buffer_load_dwordx4 v[30:33], v70, s[0:3], s5 offen nt
	s_add_i32 s5, s4, 0x40000
	buffer_load_dwordx4 v[42:45], v68, s[0:3], s5 offen nt
	s_waitcnt vmcnt(4)
	v_pk_fma_f32 v[50:51], v[14:15], v[36:37], v[50:51]
	v_pk_fma_f32 v[52:53], v[12:13], v[34:35], v[52:53]
	buffer_load_dwordx4 v[34:37], v67, s[0:3], s5 offen nt
	v_add_f32_dpp v16, v16, v16 quad_perm:[2,3,0,1] row_mask:0xf bank_mask:0xf bound_ctrl:1
	s_waitcnt vmcnt(4)
	v_pk_fma_f32 v[58:59], v[10:11], v[40:41], v[50:51]
	v_pk_fma_f32 v[38:39], v[8:9], v[38:39], v[52:53]
	v_add_f32_e32 v19, v58, v59
	v_add_f32_e32 v17, v38, v39
	v_add_f32_dpp v58, v60, v60 quad_perm:[1,0,3,2] row_mask:0xf bank_mask:0xf bound_ctrl:1
	v_add_f32_e32 v18, v17, v19
	v_add_f32_dpp v16, v16, v16 row_ror:4 row_mask:0xf bank_mask:0xf bound_ctrl:1
	v_add_f32_dpp v17, v58, v58 quad_perm:[2,3,0,1] row_mask:0xf bank_mask:0xf bound_ctrl:1
	buffer_load_dwordx4 v[20:23], v69, s[0:3], s5 offen nt
	buffer_load_dwordx4 v[46:49], v70, s[0:3], s5 offen nt
	v_add_f32_dpp v17, v17, v17 row_ror:4 row_mask:0xf bank_mask:0xf bound_ctrl:1
	v_add_f32_dpp v58, v16, v16 row_ror:8 row_mask:0xf bank_mask:0xf bound_ctrl:1
	buffer_load_dwordx4 v[38:41], v67, s[0:3], s10 offen nt
	buffer_load_dwordx4 v[50:53], v68, s[0:3], s10 offen nt
	v_add_f32_dpp v17, v17, v17 row_ror:8 row_mask:0xf bank_mask:0xf bound_ctrl:1
	v_mov_b32_e32 v19, v17
	v_mov_b32_e32 v59, v58
	s_nop 0
	v_permlane16_swap_b32_e32 v17, v19
	v_permlane16_swap_b32_e32 v58, v59
	v_add_f32_e32 v16, v17, v19
	v_add_f32_e32 v17, v58, v59
	s_add_i32 s5, s4, 0x60000
	s_add_i32 s4, s4, 0x70000
	v_add_f32_dpp v18, v18, v18 quad_perm:[1,0,3,2] row_mask:0xf bank_mask:0xf bound_ctrl:1
	s_waitcnt vmcnt(7)
	v_pk_fma_f32 v[28:29], v[14:15], v[28:29], v[54:55]
	v_pk_fma_f32 v[54:55], v[12:13], v[26:27], v[56:57]
	s_waitcnt vmcnt(6)
	v_pk_fma_f32 v[58:59], v[10:11], v[32:33], v[28:29]
	buffer_load_dwordx4 v[26:29], v69, s[0:3], s10 offen nt
	v_pk_fma_f32 v[54:55], v[8:9], v[30:31], v[54:55]
	buffer_load_dwordx4 v[30:33], v70, s[0:3], s10 offen nt
	v_add_f32_e32 v66, v54, v55
	s_waitcnt vmcnt(7)
	v_pk_mul_f32 v[54:55], v[6:7], v[44:45]
	v_pk_mul_f32 v[56:57], v[4:5], v[42:43]
	buffer_load_dwordx4 v[42:45], v68, s[0:3], s5 offen nt
	s_waitcnt vmcnt(7)
	v_pk_fma_f32 v[54:55], v[2:3], v[36:37], v[54:55]
	v_pk_fma_f32 v[56:57], v[0:1], v[34:35], v[56:57]
	buffer_load_dwordx4 v[34:37], v67, s[0:3], s5 offen nt
	v_add_f32_dpp v18, v18, v18 quad_perm:[2,3,0,1] row_mask:0xf bank_mask:0xf bound_ctrl:1
	s_waitcnt vmcnt(7)
	v_pk_fma_f32 v[22:23], v[14:15], v[22:23], v[54:55]
	v_pk_fma_f32 v[20:21], v[12:13], v[20:21], v[56:57]
	s_waitcnt vmcnt(6)
	v_pk_fma_f32 v[60:61], v[10:11], v[48:49], v[22:23]
	v_pk_fma_f32 v[22:23], v[8:9], v[46:47], v[20:21]
	s_waitcnt vmcnt(4)
	v_pk_mul_f32 v[54:55], v[4:5], v[50:51]
	v_pk_mul_f32 v[20:21], v[6:7], v[52:53]
	v_pk_fma_f32 v[38:39], v[0:1], v[38:39], v[54:55]
	buffer_load_dwordx4 v[46:49], v69, s[0:3], s5 offen nt
	buffer_load_dwordx4 v[50:53], v70, s[0:3], s5 offen nt
	v_pk_fma_f32 v[20:21], v[2:3], v[40:41], v[20:21]
	v_add_f32_e32 v23, v22, v23
	v_add_f32_dpp v18, v18, v18 row_ror:4 row_mask:0xf bank_mask:0xf bound_ctrl:1
	s_waitcnt vmcnt(5)
	v_pk_fma_f32 v[26:27], v[12:13], v[26:27], v[38:39]
	buffer_load_dwordx4 v[38:41], v67, s[0:3], s4 offen nt
	buffer_load_dwordx4 v[54:57], v68, s[0:3], s4 offen nt
	v_pk_fma_f32 v[20:21], v[14:15], v[28:29], v[20:21]
	s_waitcnt vmcnt(6)
	v_pk_fma_f32 v[30:31], v[8:9], v[30:31], v[26:27]
	v_pk_fma_f32 v[62:63], v[10:11], v[32:33], v[20:21]
	v_add_f32_dpp v18, v18, v18 row_ror:8 row_mask:0xf bank_mask:0xf bound_ctrl:1
	s_waitcnt vmcnt(5)
	v_pk_mul_f32 v[20:21], v[6:7], v[44:45]
	v_pk_mul_f32 v[26:27], v[4:5], v[42:43]
	buffer_load_dwordx4 v[42:45], v69, s[0:3], s4 offen nt
	s_waitcnt vmcnt(5)
	v_pk_fma_f32 v[64:65], v[0:1], v[34:35], v[26:27]
	buffer_load_dwordx4 v[32:35], v70, s[0:3], s4 offen nt
	v_add_f32_e32 v27, v60, v61
	v_add_f32_e32 v23, v23, v27
	v_pk_fma_f32 v[36:37], v[2:3], v[36:37], v[20:21]
	v_add_f32_e32 v20, v58, v59
	v_add_f32_dpp v23, v23, v23 quad_perm:[1,0,3,2] row_mask:0xf bank_mask:0xf bound_ctrl:1
	v_add_f32_e32 v20, v66, v20
	v_mov_b32_e32 v19, v18
	v_add_f32_dpp v23, v23, v23 quad_perm:[2,3,0,1] row_mask:0xf bank_mask:0xf bound_ctrl:1
	v_add_f32_dpp v20, v20, v20 quad_perm:[1,0,3,2] row_mask:0xf bank_mask:0xf bound_ctrl:1
	v_permlane16_swap_b32_e32 v18, v19
	v_add_f32_dpp v23, v23, v23 row_ror:4 row_mask:0xf bank_mask:0xf bound_ctrl:1
	v_add_f32_dpp v20, v20, v20 quad_perm:[2,3,0,1] row_mask:0xf bank_mask:0xf bound_ctrl:1
	v_add_f32_e32 v18, v18, v19
	v_add_f32_dpp v23, v23, v23 row_ror:8 row_mask:0xf bank_mask:0xf bound_ctrl:1
	v_mov_b32_e32 v27, v23
	s_nop 1
	v_permlane16_swap_b32_e32 v23, v27
	v_add_f32_e32 v28, v23, v27
	v_add_f32_e32 v23, v30, v31
	s_waitcnt vmcnt(5)
	v_pk_fma_f32 v[30:31], v[14:15], v[48:49], v[36:37]
	v_pk_fma_f32 v[36:37], v[12:13], v[46:47], v[64:65]
	s_waitcnt vmcnt(4)
	v_pk_fma_f32 v[30:31], v[10:11], v[52:53], v[30:31]
	v_pk_fma_f32 v[36:37], v[8:9], v[50:51], v[36:37]
	v_add_f32_e32 v27, v62, v63
	v_add_f32_e32 v36, v36, v37
	v_add_f32_e32 v30, v30, v31
	v_add_f32_e32 v23, v23, v27
	v_add_f32_e32 v30, v36, v30
	v_add_f32_dpp v20, v20, v20 row_ror:4 row_mask:0xf bank_mask:0xf bound_ctrl:1
	v_add_f32_dpp v23, v23, v23 quad_perm:[1,0,3,2] row_mask:0xf bank_mask:0xf bound_ctrl:1
	v_add_f32_dpp v30, v30, v30 quad_perm:[1,0,3,2] row_mask:0xf bank_mask:0xf bound_ctrl:1
	v_add_f32_dpp v20, v20, v20 row_ror:8 row_mask:0xf bank_mask:0xf bound_ctrl:1
	v_add_f32_dpp v23, v23, v23 quad_perm:[2,3,0,1] row_mask:0xf bank_mask:0xf bound_ctrl:1
	v_add_f32_dpp v30, v30, v30 quad_perm:[2,3,0,1] row_mask:0xf bank_mask:0xf bound_ctrl:1
	v_mov_b32_e32 v21, v20
	v_add_f32_dpp v23, v23, v23 row_ror:4 row_mask:0xf bank_mask:0xf bound_ctrl:1
	v_add_f32_dpp v30, v30, v30 row_ror:4 row_mask:0xf bank_mask:0xf bound_ctrl:1
	v_permlane16_swap_b32_e32 v20, v21
	v_add_f32_dpp v23, v23, v23 row_ror:8 row_mask:0xf bank_mask:0xf bound_ctrl:1
	v_add_f32_dpp v30, v30, v30 row_ror:8 row_mask:0xf bank_mask:0xf bound_ctrl:1
	v_mov_b32_e32 v27, v23
	v_mov_b32_e32 v31, v30
	s_nop 0
	v_permlane16_swap_b32_e32 v23, v27
	v_permlane16_swap_b32_e32 v30, v31
	v_add_f32_e32 v21, v20, v21
	v_add_f32_e32 v23, v23, v27
	v_add_f32_e32 v30, v30, v31
	v_mov_b32_e32 v19, v16
	v_mov_b32_e32 v20, v17
	v_mov_b32_e32 v22, v18
	v_mov_b32_e32 v26, v21
	v_mov_b32_e32 v29, v28
	v_mov_b32_e32 v27, v23
	v_mov_b32_e32 v31, v30
	v_permlane32_swap_b32_e32 v16, v19
	v_permlane32_swap_b32_e32 v17, v20
	v_permlane32_swap_b32_e32 v18, v22
	v_permlane32_swap_b32_e32 v21, v26
	v_permlane32_swap_b32_e32 v28, v29
	v_permlane32_swap_b32_e32 v23, v27
	s_waitcnt vmcnt(2)
	v_pk_mul_f32 v[6:7], v[6:7], v[56:57]
	v_pk_mul_f32 v[4:5], v[4:5], v[54:55]
	v_pk_fma_f32 v[2:3], v[2:3], v[40:41], v[6:7]
	v_pk_fma_f32 v[0:1], v[0:1], v[38:39], v[4:5]
	v_permlane32_swap_b32_e32 v30, v31
	s_waitcnt vmcnt(1)
	v_pk_fma_f32 v[2:3], v[14:15], v[44:45], v[2:3]
	v_pk_fma_f32 v[0:1], v[12:13], v[42:43], v[0:1]
	s_waitcnt vmcnt(0)
	v_pk_fma_f32 v[2:3], v[10:11], v[34:35], v[2:3]
	v_pk_fma_f32 v[0:1], v[8:9], v[32:33], v[0:1]
	s_nop 0
	v_add_f32_e32 v0, v0, v1
	v_add_f32_e32 v1, v2, v3
	v_add_f32_e32 v0, v0, v1
	s_nop 1
	v_add_f32_dpp v0, v0, v0 quad_perm:[1,0,3,2] row_mask:0xf bank_mask:0xf bound_ctrl:1
	s_nop 1
	v_add_f32_dpp v0, v0, v0 quad_perm:[2,3,0,1] row_mask:0xf bank_mask:0xf bound_ctrl:1
	s_nop 1
	v_add_f32_dpp v0, v0, v0 row_ror:4 row_mask:0xf bank_mask:0xf bound_ctrl:1
	s_nop 1
	v_add_f32_dpp v0, v0, v0 row_ror:8 row_mask:0xf bank_mask:0xf bound_ctrl:1
	v_mov_b32_e32 v1, v0
	s_nop 1
	v_permlane16_swap_b32_e32 v0, v1
	v_add_f32_e32 v0, v0, v1
	v_mov_b32_e32 v1, v0
	s_nop 1
	v_permlane32_swap_b32_e32 v0, v1
	s_and_saveexec_b64 s[0:1], vcc
	s_cbranch_execz .LBB1_4
	v_add_f32_e32 v6, v16, v19
	v_cmp_eq_u32_e32 vcc, 0, v24
	v_add_f32_e32 v5, v17, v20
	v_add_f32_e32 v4, v18, v22
	v_cndmask_b32_e32 v6, 0, v6, vcc
	v_cmp_eq_u32_e32 vcc, 1, v24
	v_add_f32_e32 v3, v21, v26
	v_add_f32_e32 v2, v28, v29
	v_cndmask_b32_e32 v5, v6, v5, vcc
	v_cmp_eq_u32_e32 vcc, 2, v24
	v_add_f32_e32 v0, v0, v1
	v_add_f32_e32 v1, v30, v31
	v_cndmask_b32_e32 v4, v5, v4, vcc
	v_cmp_eq_u32_e32 vcc, 3, v24
	s_lshl_b32 s0, s8, 13
	s_and_b32 s0, s0, 0x1e000
	v_cndmask_b32_e32 v3, v4, v3, vcc
	v_cmp_eq_u32_e32 vcc, 4, v24
	s_add_u32 s0, s6, s0
	s_addc_u32 s1, s7, 0
	v_cndmask_b32_e32 v2, v3, v2, vcc
	v_add_f32_e32 v3, v23, v27
	v_cmp_eq_u32_e32 vcc, 5, v24
	s_nop 1
	v_cndmask_b32_e32 v2, v2, v3, vcc
	v_cmp_eq_u32_e32 vcc, 6, v24
	s_nop 1
	v_cndmask_b32_e32 v1, v2, v1, vcc
	v_cmp_eq_u32_e32 vcc, 7, v24
	s_nop 1
	v_cndmask_b32_e32 v2, v1, v0, vcc
	v_add_u32_e32 v0, s9, v25
	v_ashrrev_i32_e32 v0, 4, v0
	v_ashrrev_i32_e32 v1, 31, v0
	v_lshl_add_u64 v[0:1], v[0:1], 2, s[0:1]
	v_add_co_u32_e32 v0, vcc, 0x6000, v0
	s_nop 1
	v_addc_co_u32_e32 v1, vcc, 0, v1, vcc
	global_store_dword v[0:1], v2, off offset:64

	.amdhsa_kernel _Z13stream_kernelPKfPf
		.amdhsa_group_segment_fixed_size 4096
		.amdhsa_private_segment_fixed_size 0
		.amdhsa_kernarg_size 16
		.amdhsa_user_sgpr_count 2
		.amdhsa_user_sgpr_dispatch_ptr 0
		.amdhsa_user_sgpr_queue_ptr 0
		.amdhsa_user_sgpr_kernarg_segment_ptr 1
		.amdhsa_user_sgpr_dispatch_id 0
		.amdhsa_user_sgpr_kernarg_preload_length 0
		.amdhsa_user_sgpr_kernarg_preload_offset 0
		.amdhsa_user_sgpr_private_segment_size 0
		.amdhsa_uses_dynamic_stack 0
		.amdhsa_enable_private_segment 0
		.amdhsa_system_sgpr_workgroup_id_x 1
		.amdhsa_system_sgpr_workgroup_id_y 0
		.amdhsa_system_sgpr_workgroup_id_z 0
		.amdhsa_system_sgpr_workgroup_info 0
		.amdhsa_system_vgpr_workitem_id 0
		.amdhsa_next_free_vgpr 71
		.amdhsa_next_free_sgpr 13
		.amdhsa_accum_offset 72
		.amdhsa_reserve_vcc 1
		.amdhsa_float_round_mode_32 0
		.amdhsa_float_round_mode_16_64 0
		.amdhsa_float_denorm_mode_32 3
		.amdhsa_float_denorm_mode_16_64 3
		.amdhsa_dx10_clamp 1
		.amdhsa_ieee_mode 1
		.amdhsa_fp16_overflow 0
		.amdhsa_tg_split 0
		.amdhsa_exception_fp_ieee_invalid_op 0
		.amdhsa_exception_fp_denorm_src 0
		.amdhsa_exception_fp_ieee_div_zero 0
		.amdhsa_exception_fp_ieee_overflow 0
		.amdhsa_exception_fp_ieee_underflow 0
		.amdhsa_exception_fp_ieee_inexact 0
		.amdhsa_exception_int_div_zero 0
	.end_amdhsa_kernel

.Lfunc_end1:
	.size	_Z13stream_kernelPKfPf, .Lfunc_end1-_Z13stream_kernelPKfPf
	.set _Z13stream_kernelPKfPf.num_vgpr, 71
	.set _Z13stream_kernelPKfPf.num_agpr, 0
	.set _Z13stream_kernelPKfPf.numbered_sgpr, 13
	.set _Z13stream_kernelPKfPf.num_named_barrier, 0
	.set _Z13stream_kernelPKfPf.private_seg_size, 0
	.set _Z13stream_kernelPKfPf.uses_vcc, 1
	.set _Z13stream_kernelPKfPf.uses_flat_scratch, 0
	.set _Z13stream_kernelPKfPf.has_dyn_sized_stack, 0
	.set _Z13stream_kernelPKfPf.has_recursion, 0
	.set _Z13stream_kernelPKfPf.has_indirect_call, 0

amdhsa.kernels:
  - .agpr_count:     0
    .args:
      - .actual_access:  read_only
        .address_space:  global
        .offset:         0
        .size:           8
        .value_kind:     global_buffer
      - .actual_access:  read_only
        .address_space:  global
        .offset:         8
        .size:           8
        .value_kind:     global_buffer
      - .actual_access:  read_only
        .address_space:  global
        .offset:         16
        .size:           8
        .value_kind:     global_buffer
      - .actual_access:  read_only
        .address_space:  global
        .offset:         24
        .size:           8
        .value_kind:     global_buffer
      - .actual_access:  write_only
        .address_space:  global
        .offset:         32
        .size:           8
        .value_kind:     global_buffer
    .group_segment_fixed_size: 2112
    .kernarg_segment_align: 8
    .kernarg_segment_size: 40
    .language:       OpenCL C
    .language_version:
      - 2
      - 0
    .max_flat_workgroup_size: 1024
    .name:           _Z11prep_kernelPKfS0_S0_S0_Pf
    .private_segment_fixed_size: 0
    .sgpr_count:     32
    .sgpr_spill_count: 0
    .symbol:         _Z11prep_kernelPKfS0_S0_S0_Pf.kd
    .uniform_work_group_size: 1
    .uses_dynamic_stack: false
    .vgpr_count:     40
    .vgpr_spill_count: 0
    .wavefront_size: 64
  - .agpr_count:     0
    .args:
      - .actual_access:  read_only
        .address_space:  global
        .offset:         0
        .size:           8
        .value_kind:     global_buffer
      - .address_space:  global
        .offset:         8
        .size:           8
        .value_kind:     global_buffer
    .group_segment_fixed_size: 4096
    .kernarg_segment_align: 8
    .kernarg_segment_size: 16
    .language:       OpenCL C
    .language_version:
      - 2
      - 0
    .max_flat_workgroup_size: 1024
    .name:           _Z13stream_kernelPKfPf
    .private_segment_fixed_size: 0
    .sgpr_count:     19
    .sgpr_spill_count: 0
    .symbol:         _Z13stream_kernelPKfPf.kd
    .uniform_work_group_size: 1
    .uses_dynamic_stack: false
    .vgpr_count:     71
    .vgpr_spill_count: 0
    .wavefront_size: 64
  - .agpr_count:     0
    .args:
      - .actual_access:  read_only
        .address_space:  global
        .offset:         0
        .size:           8
        .value_kind:     global_buffer
      - .actual_access:  write_only
        .address_space:  global
        .offset:         8
        .size:           8
        .value_kind:     global_buffer
    .group_segment_fixed_size: 32
    .kernarg_segment_align: 8
    .kernarg_segment_size: 16
    .language:       OpenCL C
    .language_version:
      - 2
      - 0
    .max_flat_workgroup_size: 256
    .name:           _Z14softmax_kernelPKfPf
    .private_segment_fixed_size: 0
    .sgpr_count:     16
    .sgpr_spill_count: 0
    .symbol:         _Z14softmax_kernelPKfPf.kd
    .uniform_work_group_size: 1
    .uses_dynamic_stack: false
    .vgpr_count:     17
    .vgpr_spill_count: 0
    .wavefront_size: 64
